# K3: overflow words of >64 dst segments loaded with the main batch into 4 slots; slow serial paths only for >4 long segments per wave
# speedup vs baseline: 1.0359x; 1.0035x over previous
.LBB2_14:
	s_or_b64 exec, exec, s[2:3]
	s_and_saveexec_b64 s[2:3], s[4:5]
	s_movk_i32 s6, 0x30d4
	v_lshlrev_b32_e32 v5, 2, v102
	v_add_u32_e32 v7, 0x17850, v5
	v_add_u32_e32 v5, 0x17450, v5
	v_mad_u32_u24 v1, v102, s6, v2
	v_sub_u32_e32 v8, v3, v2
	ds_write_b32 v7, v1
	ds_write_b32 v5, v8
	s_or_b64 exec, exec, s[2:3]
	v_readfirstlane_b32 s86, v6
	v_lshlrev_b32_e32 v48, 4, v6
	v_lshlrev_b32_e32 v83, 2, v45
	s_mul_i32 s86, s86, 0xc3500
	s_add_u32 s86, s46, s86
	s_addc_u32 s87, s47, 0
	s_mov_b32 s94, 0
	s_mov_b32 s75, 0
	s_mov_b32 s82, 0
	s_mov_b32 s95, 0
	s_mov_b32 s32, 0
	v_readlane_b32 s2, v2, 0
	v_readlane_b32 s3, v3, 0
	v_readlane_b32 s84, v2, 1
	v_readlane_b32 s85, v3, 1
	s_sub_i32 s42, s3, s2
	s_lshl_b32 s2, s2, 2
	s_add_u32 s88, s86, s2
	s_addc_u32 s89, s87, 0
	v_cmp_gt_u32_e64 s[20:21], s42, v45
	global_load_dword v18, v83, s[88:89]
	s_cmp_le_u32 s42, 64
	s_cbranch_scc1 .Lag_n0
	s_cmp_eq_u32 s94, 0
	s_cbranch_scc0 .Lag_0_1
	s_add_u32 s76, s88, 0x100
	s_addc_u32 s77, s89, 0
	s_sub_i32 s75, s42, 64
	s_branch .Lag_0_e
.Lag_0_1:
	s_cmp_eq_u32 s94, 1
	s_cbranch_scc0 .Lag_0_2
	s_add_u32 s78, s88, 0x100
	s_addc_u32 s79, s89, 0
	s_sub_i32 s82, s42, 64
	s_branch .Lag_0_e
.Lag_0_2:
	s_cmp_eq_u32 s94, 2
	s_cbranch_scc0 .Lag_0_3
	s_add_u32 s80, s88, 0x100
	s_addc_u32 s81, s89, 0
	s_sub_i32 s95, s42, 64
	s_branch .Lag_0_e
.Lag_0_3:
	s_cmp_eq_u32 s94, 3
	s_cbranch_scc0 .Lag_0_e
	s_add_u32 s92, s88, 0x100
	s_addc_u32 s93, s89, 0
	s_sub_i32 s32, s42, 64
.Lag_0_e:
	s_add_i32 s94, s94, 1
.Lag_n0:
	s_add_u32 s86, s86, 0xc350
	s_addc_u32 s87, s87, 0
	v_readlane_b32 s2, v2, 2
	v_readlane_b32 s3, v3, 2
	s_sub_i32 s50, s85, s84
	s_lshl_b32 s84, s84, 2
	s_add_u32 s90, s86, s84
	s_addc_u32 s91, s87, 0
	v_cmp_gt_u32_e64 s[8:9], s50, v45
	global_load_dword v16, v83, s[90:91]
	s_cmp_le_u32 s50, 64
	s_cbranch_scc1 .Lag_n1
	s_cmp_eq_u32 s94, 0
	s_cbranch_scc0 .Lag_1_1
	s_add_u32 s76, s90, 0x100
	s_addc_u32 s77, s91, 0
	s_sub_i32 s75, s50, 64
	s_branch .Lag_1_e
.Lag_1_1:
	s_cmp_eq_u32 s94, 1
	s_cbranch_scc0 .Lag_1_2
	s_add_u32 s78, s90, 0x100
	s_addc_u32 s79, s91, 0
	s_sub_i32 s82, s50, 64
	s_branch .Lag_1_e
.Lag_1_2:
	s_cmp_eq_u32 s94, 2
	s_cbranch_scc0 .Lag_1_3
	s_add_u32 s80, s90, 0x100
	s_addc_u32 s81, s91, 0
	s_sub_i32 s95, s50, 64
	s_branch .Lag_1_e
.Lag_1_3:
	s_cmp_eq_u32 s94, 3
	s_cbranch_scc0 .Lag_1_e
	s_add_u32 s92, s90, 0x100
	s_addc_u32 s93, s91, 0
	s_sub_i32 s32, s50, 64

.Lag_n1:
	s_add_u32 s86, s86, 0xc350
	s_addc_u32 s87, s87, 0
	v_readlane_b32 s84, v2, 3
	v_readlane_b32 s85, v3, 3
	s_sub_i32 s48, s3, s2
	s_lshl_b32 s2, s2, 2
	s_add_u32 s88, s86, s2
	s_addc_u32 s89, s87, 0
	v_cmp_gt_u32_e64 s[10:11], s48, v45
	global_load_dword v14, v83, s[88:89]
	s_cmp_le_u32 s48, 64
	s_cbranch_scc1 .Lag_n2
	s_cmp_eq_u32 s94, 0
	s_cbranch_scc0 .Lag_2_1
	s_add_u32 s76, s88, 0x100
	s_addc_u32 s77, s89, 0
	s_sub_i32 s75, s48, 64
	s_branch .Lag_2_e
.Lag_2_1:
	s_cmp_eq_u32 s94, 1
	s_cbranch_scc0 .Lag_2_2
	s_add_u32 s78, s88, 0x100
	s_addc_u32 s79, s89, 0
	s_sub_i32 s82, s48, 64
	s_branch .Lag_2_e
.Lag_2_2:
	s_cmp_eq_u32 s94, 2
	s_cbranch_scc0 .Lag_2_3
	s_add_u32 s80, s88, 0x100
	s_addc_u32 s81, s89, 0
	s_sub_i32 s95, s48, 64
	s_branch .Lag_2_e
.Lag_2_3:
	s_cmp_eq_u32 s94, 3
	s_cbranch_scc0 .Lag_2_e
	s_add_u32 s92, s88, 0x100
	s_addc_u32 s93, s89, 0
	s_sub_i32 s32, s48, 64

.Lag_n2:
	s_add_u32 s86, s86, 0xc350
	s_addc_u32 s87, s87, 0
	v_readlane_b32 s2, v2, 4
	v_readlane_b32 s3, v3, 4
	s_sub_i32 s43, s85, s84
	s_lshl_b32 s84, s84, 2
	s_add_u32 s90, s86, s84
	s_addc_u32 s91, s87, 0
	v_cmp_gt_u32_e64 s[12:13], s43, v45
	global_load_dword v13, v83, s[90:91]
	s_cmp_le_u32 s43, 64
	s_cbranch_scc1 .Lag_n3
	s_cmp_eq_u32 s94, 0
	s_cbranch_scc0 .Lag_3_1
	s_add_u32 s76, s90, 0x100
	s_addc_u32 s77, s91, 0
	s_sub_i32 s75, s43, 64
	s_branch .Lag_3_e
.Lag_3_1:
	s_cmp_eq_u32 s94, 1
	s_cbranch_scc0 .Lag_3_2
	s_add_u32 s78, s90, 0x100
	s_addc_u32 s79, s91, 0
	s_sub_i32 s82, s43, 64
	s_branch .Lag_3_e
.Lag_3_2:
	s_cmp_eq_u32 s94, 2
	s_cbranch_scc0 .Lag_3_3
	s_add_u32 s80, s90, 0x100
	s_addc_u32 s81, s91, 0
	s_sub_i32 s95, s43, 64
	s_branch .Lag_3_e
.Lag_3_3:
	s_cmp_eq_u32 s94, 3
	s_cbranch_scc0 .Lag_3_e
	s_add_u32 s92, s90, 0x100
	s_addc_u32 s93, s91, 0
	s_sub_i32 s32, s43, 64

.Lag_n3:
	s_add_u32 s86, s86, 0xc350
	s_addc_u32 s87, s87, 0
	v_readlane_b32 s84, v2, 5
	v_readlane_b32 s85, v3, 5
	s_sub_i32 s51, s3, s2
	s_lshl_b32 s2, s2, 2
	s_add_u32 s88, s86, s2
	s_addc_u32 s89, s87, 0
	v_cmp_gt_u32_e64 s[14:15], s51, v45
	global_load_dword v11, v83, s[88:89]
	s_cmp_le_u32 s51, 64
	s_cbranch_scc1 .Lag_n4
	s_cmp_eq_u32 s94, 0
	s_cbranch_scc0 .Lag_4_1
	s_add_u32 s76, s88, 0x100
	s_addc_u32 s77, s89, 0
	s_sub_i32 s75, s51, 64
	s_branch .Lag_4_e
.Lag_4_1:
	s_cmp_eq_u32 s94, 1
	s_cbranch_scc0 .Lag_4_2
	s_add_u32 s78, s88, 0x100
	s_addc_u32 s79, s89, 0
	s_sub_i32 s82, s51, 64
	s_branch .Lag_4_e
.Lag_4_2:
	s_cmp_eq_u32 s94, 2
	s_cbranch_scc0 .Lag_4_3
	s_add_u32 s80, s88, 0x100
	s_addc_u32 s81, s89, 0
	s_sub_i32 s95, s51, 64
	s_branch .Lag_4_e
.Lag_4_3:
	s_cmp_eq_u32 s94, 3
	s_cbranch_scc0 .Lag_4_e
	s_add_u32 s92, s88, 0x100
	s_addc_u32 s93, s89, 0
	s_sub_i32 s32, s51, 64

.Lag_n4:
	s_add_u32 s86, s86, 0xc350
	s_addc_u32 s87, s87, 0
	v_readlane_b32 s2, v2, 6
	v_readlane_b32 s3, v3, 6
	s_sub_i32 s49, s85, s84
	s_lshl_b32 s84, s84, 2
	s_add_u32 s90, s86, s84
	s_addc_u32 s91, s87, 0
	v_cmp_gt_u32_e64 s[16:17], s49, v45
	global_load_dword v9, v83, s[90:91]
	s_cmp_le_u32 s49, 64
	s_cbranch_scc1 .Lag_n5
	s_cmp_eq_u32 s94, 0
	s_cbranch_scc0 .Lag_5_1
	s_add_u32 s76, s90, 0x100
	s_addc_u32 s77, s91, 0
	s_sub_i32 s75, s49, 64
	s_branch .Lag_5_e
.Lag_5_1:
	s_cmp_eq_u32 s94, 1
	s_cbranch_scc0 .Lag_5_2
	s_add_u32 s78, s90, 0x100
	s_addc_u32 s79, s91, 0
	s_sub_i32 s82, s49, 64
	s_branch .Lag_5_e
.Lag_5_2:
	s_cmp_eq_u32 s94, 2
	s_cbranch_scc0 .Lag_5_3
	s_add_u32 s80, s90, 0x100
	s_addc_u32 s81, s91, 0
	s_sub_i32 s95, s49, 64
	s_branch .Lag_5_e
.Lag_5_3:
	s_cmp_eq_u32 s94, 3
	s_cbranch_scc0 .Lag_5_e
	s_add_u32 s92, s90, 0x100
	s_addc_u32 s93, s91, 0
	s_sub_i32 s32, s49, 64

.Lag_n5:
	s_add_u32 s86, s86, 0xc350
	s_addc_u32 s87, s87, 0
	v_readlane_b32 s84, v2, 7
	v_readlane_b32 s85, v3, 7
	s_sub_i32 s66, s3, s2
	s_lshl_b32 s2, s2, 2
	s_add_u32 s88, s86, s2
	s_addc_u32 s89, s87, 0
	v_cmp_gt_u32_e64 s[18:19], s66, v45
	global_load_dword v8, v83, s[88:89]
	s_cmp_le_u32 s66, 64
	s_cbranch_scc1 .Lag_n6
	s_cmp_eq_u32 s94, 0
	s_cbranch_scc0 .Lag_6_1
	s_add_u32 s76, s88, 0x100
	s_addc_u32 s77, s89, 0
	s_sub_i32 s75, s66, 64
	s_branch .Lag_6_e
.Lag_6_1:
	s_cmp_eq_u32 s94, 1
	s_cbranch_scc0 .Lag_6_2
	s_add_u32 s78, s88, 0x100
	s_addc_u32 s79, s89, 0
	s_sub_i32 s82, s66, 64
	s_branch .Lag_6_e
.Lag_6_2:
	s_cmp_eq_u32 s94, 2
	s_cbranch_scc0 .Lag_6_3
	s_add_u32 s80, s88, 0x100
	s_addc_u32 s81, s89, 0
	s_sub_i32 s95, s66, 64
	s_branch .Lag_6_e
.Lag_6_3:
	s_cmp_eq_u32 s94, 3
	s_cbranch_scc0 .Lag_6_e
	s_add_u32 s92, s88, 0x100
	s_addc_u32 s93, s89, 0
	s_sub_i32 s32, s66, 64

.Lag_n6:
	s_add_u32 s86, s86, 0xc350
	s_addc_u32 s87, s87, 0
	v_readlane_b32 s2, v2, 8
	v_readlane_b32 s3, v3, 8
	s_sub_i32 s65, s85, s84
	s_lshl_b32 s84, s84, 2
	s_add_u32 s90, s86, s84
	s_addc_u32 s91, s87, 0
	v_cmp_gt_u32_e64 s[22:23], s65, v45
	global_load_dword v7, v83, s[90:91]
	s_cmp_le_u32 s65, 64
	s_cbranch_scc1 .Lag_n7
	s_cmp_eq_u32 s94, 0
	s_cbranch_scc0 .Lag_7_1
	s_add_u32 s76, s90, 0x100
	s_addc_u32 s77, s91, 0
	s_sub_i32 s75, s65, 64
	s_branch .Lag_7_e
.Lag_7_1:
	s_cmp_eq_u32 s94, 1
	s_cbranch_scc0 .Lag_7_2
	s_add_u32 s78, s90, 0x100
	s_addc_u32 s79, s91, 0
	s_sub_i32 s82, s65, 64
	s_branch .Lag_7_e
.Lag_7_2:
	s_cmp_eq_u32 s94, 2
	s_cbranch_scc0 .Lag_7_3
	s_add_u32 s80, s90, 0x100
	s_addc_u32 s81, s91, 0
	s_sub_i32 s95, s65, 64
	s_branch .Lag_7_e
.Lag_7_3:
	s_cmp_eq_u32 s94, 3
	s_cbranch_scc0 .Lag_7_e
	s_add_u32 s92, s90, 0x100
	s_addc_u32 s93, s91, 0
	s_sub_i32 s32, s65, 64

.Lag_n7:
	s_add_u32 s86, s86, 0xc350
	s_addc_u32 s87, s87, 0
	v_readlane_b32 s84, v2, 9
	v_readlane_b32 s85, v3, 9
	s_sub_i32 s68, s3, s2
	s_lshl_b32 s2, s2, 2
	s_add_u32 s88, s86, s2
	s_addc_u32 s89, s87, 0
	v_cmp_gt_u32_e64 s[24:25], s68, v45
	global_load_dword v17, v83, s[88:89]
	s_cmp_le_u32 s68, 64
	s_cbranch_scc1 .Lag_n8
	s_cmp_eq_u32 s94, 0
	s_cbranch_scc0 .Lag_8_1
	s_add_u32 s76, s88, 0x100
	s_addc_u32 s77, s89, 0
	s_sub_i32 s75, s68, 64
	s_branch .Lag_8_e
.Lag_8_1:
	s_cmp_eq_u32 s94, 1
	s_cbranch_scc0 .Lag_8_2
	s_add_u32 s78, s88, 0x100
	s_addc_u32 s79, s89, 0
	s_sub_i32 s82, s68, 64
	s_branch .Lag_8_e
.Lag_8_2:
	s_cmp_eq_u32 s94, 2
	s_cbranch_scc0 .Lag_8_3
	s_add_u32 s80, s88, 0x100
	s_addc_u32 s81, s89, 0
	s_sub_i32 s95, s68, 64
	s_branch .Lag_8_e
.Lag_8_3:
	s_cmp_eq_u32 s94, 3
	s_cbranch_scc0 .Lag_8_e
	s_add_u32 s92, s88, 0x100
	s_addc_u32 s93, s89, 0
	s_sub_i32 s32, s68, 64

.Lag_n8:
	s_add_u32 s86, s86, 0xc350
	s_addc_u32 s87, s87, 0
	v_readlane_b32 s2, v2, 10
	v_readlane_b32 s3, v3, 10
	s_sub_i32 s67, s85, s84
	s_lshl_b32 s84, s84, 2
	s_add_u32 s90, s86, s84
	s_addc_u32 s91, s87, 0
	v_cmp_gt_u32_e64 s[26:27], s67, v45
	global_load_dword v15, v83, s[90:91]
	s_cmp_le_u32 s67, 64
	s_cbranch_scc1 .Lag_n9
	s_cmp_eq_u32 s94, 0
	s_cbranch_scc0 .Lag_9_1
	s_add_u32 s76, s90, 0x100
	s_addc_u32 s77, s91, 0
	s_sub_i32 s75, s67, 64
	s_branch .Lag_9_e
.Lag_9_1:
	s_cmp_eq_u32 s94, 1
	s_cbranch_scc0 .Lag_9_2
	s_add_u32 s78, s90, 0x100
	s_addc_u32 s79, s91, 0
	s_sub_i32 s82, s67, 64
	s_branch .Lag_9_e
.Lag_9_2:
	s_cmp_eq_u32 s94, 2
	s_cbranch_scc0 .Lag_9_3
	s_add_u32 s80, s90, 0x100
	s_addc_u32 s81, s91, 0
	s_sub_i32 s95, s67, 64
	s_branch .Lag_9_e
.Lag_9_3:
	s_cmp_eq_u32 s94, 3
	s_cbranch_scc0 .Lag_9_e
	s_add_u32 s92, s90, 0x100
	s_addc_u32 s93, s91, 0
	s_sub_i32 s32, s67, 64

.Lag_n9:
	s_add_u32 s86, s86, 0xc350
	s_addc_u32 s87, s87, 0
	v_readlane_b32 s84, v2, 11
	v_readlane_b32 s85, v3, 11
	s_sub_i32 s70, s3, s2
	s_lshl_b32 s2, s2, 2
	s_add_u32 s88, s86, s2
	s_addc_u32 s89, s87, 0
	v_cmp_gt_u32_e64 s[28:29], s70, v45
	global_load_dword v12, v83, s[88:89]
	s_cmp_le_u32 s70, 64
	s_cbranch_scc1 .Lag_n10
	s_cmp_eq_u32 s94, 0
	s_cbranch_scc0 .Lag_10_1
	s_add_u32 s76, s88, 0x100
	s_addc_u32 s77, s89, 0
	s_sub_i32 s75, s70, 64
	s_branch .Lag_10_e
.Lag_10_1:
	s_cmp_eq_u32 s94, 1
	s_cbranch_scc0 .Lag_10_2
	s_add_u32 s78, s88, 0x100
	s_addc_u32 s79, s89, 0
	s_sub_i32 s82, s70, 64
	s_branch .Lag_10_e
.Lag_10_2:
	s_cmp_eq_u32 s94, 2
	s_cbranch_scc0 .Lag_10_3
	s_add_u32 s80, s88, 0x100
	s_addc_u32 s81, s89, 0
	s_sub_i32 s95, s70, 64
	s_branch .Lag_10_e
.Lag_10_3:
	s_cmp_eq_u32 s94, 3
	s_cbranch_scc0 .Lag_10_e
	s_add_u32 s92, s88, 0x100
	s_addc_u32 s93, s89, 0
	s_sub_i32 s32, s70, 64

.Lag_n10:
	s_add_u32 s86, s86, 0xc350
	s_addc_u32 s87, s87, 0
	v_readlane_b32 s2, v2, 12
	v_readlane_b32 s3, v3, 12
	s_sub_i32 s69, s85, s84
	s_lshl_b32 s84, s84, 2
	s_add_u32 s90, s86, s84
	s_addc_u32 s91, s87, 0
	v_cmp_gt_u32_e64 s[30:31], s69, v45
	global_load_dword v10, v83, s[90:91]
	s_cmp_le_u32 s69, 64
	s_cbranch_scc1 .Lag_n11
	s_cmp_eq_u32 s94, 0
	s_cbranch_scc0 .Lag_11_1
	s_add_u32 s76, s90, 0x100
	s_addc_u32 s77, s91, 0
	s_sub_i32 s75, s69, 64
	s_branch .Lag_11_e
.Lag_11_1:
	s_cmp_eq_u32 s94, 1
	s_cbranch_scc0 .Lag_11_2
	s_add_u32 s78, s90, 0x100
	s_addc_u32 s79, s91, 0
	s_sub_i32 s82, s69, 64
	s_branch .Lag_11_e
.Lag_11_2:
	s_cmp_eq_u32 s94, 2
	s_cbranch_scc0 .Lag_11_3
	s_add_u32 s80, s90, 0x100
	s_addc_u32 s81, s91, 0
	s_sub_i32 s95, s69, 64
	s_branch .Lag_11_e
.Lag_11_3:
	s_cmp_eq_u32 s94, 3
	s_cbranch_scc0 .Lag_11_e
	s_add_u32 s92, s90, 0x100
	s_addc_u32 s93, s91, 0
	s_sub_i32 s32, s69, 64

.Lag_n11:
	s_add_u32 s86, s86, 0xc350
	s_addc_u32 s87, s87, 0
	v_readlane_b32 s84, v2, 13
	v_readlane_b32 s85, v3, 13
	s_sub_i32 s72, s3, s2
	s_lshl_b32 s2, s2, 2
	s_add_u32 s88, s86, s2
	s_addc_u32 s89, s87, 0
	v_cmp_gt_u32_e64 s[34:35], s72, v45
	global_load_dword v5, v83, s[88:89]
	s_cmp_le_u32 s72, 64
	s_cbranch_scc1 .Lag_n12
	s_cmp_eq_u32 s94, 0
	s_cbranch_scc0 .Lag_12_1
	s_add_u32 s76, s88, 0x100
	s_addc_u32 s77, s89, 0
	s_sub_i32 s75, s72, 64
	s_branch .Lag_12_e
.Lag_12_1:
	s_cmp_eq_u32 s94, 1
	s_cbranch_scc0 .Lag_12_2
	s_add_u32 s78, s88, 0x100
	s_addc_u32 s79, s89, 0
	s_sub_i32 s82, s72, 64
	s_branch .Lag_12_e
.Lag_12_2:
	s_cmp_eq_u32 s94, 2
	s_cbranch_scc0 .Lag_12_3
	s_add_u32 s80, s88, 0x100
	s_addc_u32 s81, s89, 0
	s_sub_i32 s95, s72, 64
	s_branch .Lag_12_e
.Lag_12_3:
	s_cmp_eq_u32 s94, 3
	s_cbranch_scc0 .Lag_12_e
	s_add_u32 s92, s88, 0x100
	s_addc_u32 s93, s89, 0
	s_sub_i32 s32, s72, 64

.Lag_n12:
	s_add_u32 s86, s86, 0xc350
	s_addc_u32 s87, s87, 0
	v_readlane_b32 s2, v2, 14
	v_readlane_b32 s3, v3, 14
	s_sub_i32 s71, s85, s84
	s_lshl_b32 s84, s84, 2
	s_add_u32 s90, s86, s84
	s_addc_u32 s91, s87, 0
	v_cmp_gt_u32_e64 s[36:37], s71, v45
	global_load_dword v4, v83, s[90:91]
	s_cmp_le_u32 s71, 64
	s_cbranch_scc1 .Lag_n13
	s_cmp_eq_u32 s94, 0
	s_cbranch_scc0 .Lag_13_1
	s_add_u32 s76, s90, 0x100
	s_addc_u32 s77, s91, 0
	s_sub_i32 s75, s71, 64
	s_branch .Lag_13_e
.Lag_13_1:
	s_cmp_eq_u32 s94, 1
	s_cbranch_scc0 .Lag_13_2
	s_add_u32 s78, s90, 0x100
	s_addc_u32 s79, s91, 0
	s_sub_i32 s82, s71, 64
	s_branch .Lag_13_e
.Lag_13_2:
	s_cmp_eq_u32 s94, 2
	s_cbranch_scc0 .Lag_13_3
	s_add_u32 s80, s90, 0x100
	s_addc_u32 s81, s91, 0
	s_sub_i32 s95, s71, 64
	s_branch .Lag_13_e
.Lag_13_3:
	s_cmp_eq_u32 s94, 3
	s_cbranch_scc0 .Lag_13_e
	s_add_u32 s92, s90, 0x100
	s_addc_u32 s93, s91, 0
	s_sub_i32 s32, s71, 64

.Lag_n13:
	s_add_u32 s86, s86, 0xc350
	s_addc_u32 s87, s87, 0
	v_readlane_b32 s84, v2, 15
	v_readlane_b32 s85, v3, 15
	s_sub_i32 s74, s3, s2
	s_lshl_b32 s2, s2, 2
	s_add_u32 s88, s86, s2
	s_addc_u32 s89, s87, 0
	v_cmp_gt_u32_e64 s[6:7], s74, v45
	global_load_dword v3, v83, s[88:89]
	s_cmp_le_u32 s74, 64
	s_cbranch_scc1 .Lag_n14
	s_cmp_eq_u32 s94, 0
	s_cbranch_scc0 .Lag_14_1
	s_add_u32 s76, s88, 0x100
	s_addc_u32 s77, s89, 0
	s_sub_i32 s75, s74, 64
	s_branch .Lag_14_e
.Lag_14_1:
	s_cmp_eq_u32 s94, 1
	s_cbranch_scc0 .Lag_14_2
	s_add_u32 s78, s88, 0x100
	s_addc_u32 s79, s89, 0
	s_sub_i32 s82, s74, 64
	s_branch .Lag_14_e
.Lag_14_2:
	s_cmp_eq_u32 s94, 2
	s_cbranch_scc0 .Lag_14_3
	s_add_u32 s80, s88, 0x100
	s_addc_u32 s81, s89, 0
	s_sub_i32 s95, s74, 64
	s_branch .Lag_14_e
.Lag_14_3:
	s_cmp_eq_u32 s94, 3
	s_cbranch_scc0 .Lag_14_e
	s_add_u32 s92, s88, 0x100
	s_addc_u32 s93, s89, 0
	s_sub_i32 s32, s74, 64

.Lag_n14:
	s_add_u32 s86, s86, 0xc350
	s_addc_u32 s87, s87, 0
	s_sub_i32 s73, s85, s84
	s_lshl_b32 s84, s84, 2
	s_add_u32 s90, s86, s84
	s_addc_u32 s91, s87, 0
	v_cmp_gt_u32_e32 vcc, s73, v45
	global_load_dword v2, v83, s[90:91]
	s_cmp_le_u32 s73, 64
	s_cbranch_scc1 .Lag_n15
	s_cmp_eq_u32 s94, 0
	s_cbranch_scc0 .Lag_15_1
	s_add_u32 s76, s90, 0x100
	s_addc_u32 s77, s91, 0
	s_sub_i32 s75, s73, 64
	s_branch .Lag_15_e
.Lag_15_1:
	s_cmp_eq_u32 s94, 1
	s_cbranch_scc0 .Lag_15_2
	s_add_u32 s78, s90, 0x100
	s_addc_u32 s79, s91, 0
	s_sub_i32 s82, s73, 64
	s_branch .Lag_15_e
.Lag_15_2:
	s_cmp_eq_u32 s94, 2
	s_cbranch_scc0 .Lag_15_3
	s_add_u32 s80, s90, 0x100
	s_addc_u32 s81, s91, 0
	s_sub_i32 s95, s73, 64
	s_branch .Lag_15_e
.Lag_15_3:
	s_cmp_eq_u32 s94, 3
	s_cbranch_scc0 .Lag_15_e
	s_add_u32 s92, s90, 0x100
	s_addc_u32 s93, s91, 0
	s_sub_i32 s32, s73, 64

.Lag_n15:
	s_max_u32 s84, s42, s50
	s_max_u32 s84, s84, s48
	s_max_u32 s84, s84, s43
	s_max_u32 s84, s84, s51
	s_max_u32 s84, s84, s49
	s_max_u32 s84, s84, s66
	s_max_u32 s84, s84, s65
	s_max_u32 s84, s84, s68
	s_max_u32 s84, s84, s67
	s_max_u32 s84, s84, s70
	s_max_u32 s84, s84, s69
	s_max_u32 s84, s84, s72
	s_max_u32 s84, s84, s71
	s_max_u32 s84, s84, s74
	s_max_u32 s84, s84, s73
	s_cmp_gt_u32 s84, 0x80
	s_cselect_b32 s84, 1, 0
	s_cmp_gt_u32 s94, 4
	s_cselect_b32 s85, 1, 0
	s_or_b32 s94, s84, s85
	s_cmp_lg_u32 s94, 0
	s_cbranch_scc0 .Lag_slots
	s_mov_b32 s75, 0
	s_mov_b32 s82, 0
	s_mov_b32 s95, 0
	s_mov_b32 s32, 0
	s_branch .Lag_done
.Lag_slots:
	s_cmp_eq_u32 s75, 0
	s_cbranch_scc1 .Lag_done
	v_cmp_gt_u32_e64 s[88:89], s75, v45
	s_mov_b64 exec, s[88:89]
	global_load_dword v113, v83, s[76:77]
	s_mov_b64 exec, -1
	s_cmp_eq_u32 s82, 0
	s_cbranch_scc1 .Lag_done
	v_cmp_gt_u32_e64 s[88:89], s82, v45
	s_mov_b64 exec, s[88:89]
	global_load_dword v114, v83, s[78:79]
	s_mov_b64 exec, -1
	s_cmp_eq_u32 s95, 0
	s_cbranch_scc1 .Lag_done
	v_cmp_gt_u32_e64 s[88:89], s95, v45
	s_mov_b64 exec, s[88:89]
	global_load_dword v115, v83, s[80:81]
	s_mov_b64 exec, -1
	s_cmp_eq_u32 s32, 0
	s_cbranch_scc1 .Lag_done
	v_cmp_gt_u32_e64 s[88:89], s32, v45
	s_mov_b64 exec, s[88:89]
	global_load_dword v116, v83, s[92:93]
	s_mov_b64 exec, -1
.Lag_done:
	s_barrier
	s_getreg_b32 s2, hwreg(HW_REG_XCC_ID, 0, 4)
	s_and_b32 s33, s2, 15
	s_and_saveexec_b64 s[38:39], s[44:45]
	s_cbranch_execz .LBB2_17
	s_mov_b64 s[40:41], exec
	v_mbcnt_lo_u32_b32 v19, s40, 0
	v_mbcnt_hi_u32_b32 v19, s41, v19
	v_cmp_eq_u32_e64 s[2:3], 0, v19
	s_and_b64 s[2:3], exec, s[2:3]
	s_mov_b64 exec, s[2:3]
	s_cbranch_execz .LBB2_17
	s_lshl_b32 s2, s33, 8
	s_bcnt1_i32_b64 s3, s[40:41]
	v_mov_b32_e32 v19, s2
	v_mov_b32_e32 v20, s3
	global_atomic_add v19, v20, s[54:55] offset:1024
.LBB2_17:
	s_or_b64 exec, exec, s[38:39]
	s_mov_b64 s[2:3], exec
	v_mov_b32_e32 v100, 1
	s_waitcnt vmcnt(15)
	v_cndmask_b32_e64 v19, -1, v18, s[20:21]
	v_mul_u32_u24_e32 v18, 0x640, v6
	v_or_b32_e32 v18, 0x10000, v18
	s_and_b64 exec, s[2:3], s[20:21]
	v_lshrrev_b32_e32 v84, 15, v19
	v_and_b32_e32 v84, 0x1fffc, v84
	v_add_u32_e32 v84, v18, v84
	ds_add_u32 v84, v100
	s_mov_b64 exec, s[2:3]
	s_waitcnt vmcnt(14)
	v_cndmask_b32_e64 v20, -1, v16, s[8:9]
	s_and_b64 exec, s[2:3], s[8:9]
	v_lshrrev_b32_e32 v85, 15, v20
	v_and_b32_e32 v85, 0x1fffc, v85
	v_add_u32_e32 v85, v18, v85
	ds_add_u32 v85, v100
	s_mov_b64 exec, s[2:3]
	s_waitcnt vmcnt(13)
	v_cndmask_b32_e64 v21, -1, v14, s[10:11]
	s_and_b64 exec, s[2:3], s[10:11]
	v_lshrrev_b32_e32 v86, 15, v21
	v_and_b32_e32 v86, 0x1fffc, v86
	v_add_u32_e32 v86, v18, v86
	ds_add_u32 v86, v100
	s_mov_b64 exec, s[2:3]
	s_waitcnt vmcnt(12)
	v_cndmask_b32_e64 v22, -1, v13, s[12:13]
	s_and_b64 exec, s[2:3], s[12:13]
	v_lshrrev_b32_e32 v87, 15, v22
	v_and_b32_e32 v87, 0x1fffc, v87
	v_add_u32_e32 v87, v18, v87
	ds_add_u32 v87, v100
	s_mov_b64 exec, s[2:3]
	s_waitcnt vmcnt(11)
	v_cndmask_b32_e64 v23, -1, v11, s[14:15]
	s_and_b64 exec, s[2:3], s[14:15]
	v_lshrrev_b32_e32 v88, 15, v23
	v_and_b32_e32 v88, 0x1fffc, v88
	v_add_u32_e32 v88, v18, v88
	ds_add_u32 v88, v100
	s_mov_b64 exec, s[2:3]
	s_waitcnt vmcnt(10)
	v_cndmask_b32_e64 v24, -1, v9, s[16:17]
	s_and_b64 exec, s[2:3], s[16:17]
	v_lshrrev_b32_e32 v89, 15, v24
	v_and_b32_e32 v89, 0x1fffc, v89
	v_add_u32_e32 v89, v18, v89
	ds_add_u32 v89, v100
	s_mov_b64 exec, s[2:3]
	s_waitcnt vmcnt(9)
	v_cndmask_b32_e64 v25, -1, v8, s[18:19]
	s_and_b64 exec, s[2:3], s[18:19]
	v_lshrrev_b32_e32 v90, 15, v25
	v_and_b32_e32 v90, 0x1fffc, v90
	v_add_u32_e32 v90, v18, v90
	ds_add_u32 v90, v100
	s_mov_b64 exec, s[2:3]
	s_waitcnt vmcnt(8)
	v_cndmask_b32_e64 v26, -1, v7, s[22:23]
	s_and_b64 exec, s[2:3], s[22:23]
	v_lshrrev_b32_e32 v91, 15, v26
	v_and_b32_e32 v91, 0x1fffc, v91
	v_add_u32_e32 v91, v18, v91
	ds_add_u32 v91, v100
	s_mov_b64 exec, s[2:3]
	s_waitcnt vmcnt(7)
	v_cndmask_b32_e64 v27, -1, v17, s[24:25]
	s_and_b64 exec, s[2:3], s[24:25]
	v_lshrrev_b32_e32 v92, 15, v27
	v_and_b32_e32 v92, 0x1fffc, v92
	v_add_u32_e32 v92, v18, v92
	ds_add_u32 v92, v100
	s_mov_b64 exec, s[2:3]
	s_waitcnt vmcnt(6)
	v_cndmask_b32_e64 v28, -1, v15, s[26:27]
	s_and_b64 exec, s[2:3], s[26:27]
	v_lshrrev_b32_e32 v93, 15, v28
	v_and_b32_e32 v93, 0x1fffc, v93
	v_add_u32_e32 v93, v18, v93
	ds_add_u32 v93, v100
	s_mov_b64 exec, s[2:3]
	s_waitcnt vmcnt(5)
	v_cndmask_b32_e64 v29, -1, v12, s[28:29]
	s_and_b64 exec, s[2:3], s[28:29]
	v_lshrrev_b32_e32 v94, 15, v29
	v_and_b32_e32 v94, 0x1fffc, v94
	v_add_u32_e32 v94, v18, v94
	ds_add_u32 v94, v100
	s_mov_b64 exec, s[2:3]
	s_waitcnt vmcnt(4)
	v_cndmask_b32_e64 v30, -1, v10, s[30:31]
	s_and_b64 exec, s[2:3], s[30:31]
	v_lshrrev_b32_e32 v95, 15, v30
	v_and_b32_e32 v95, 0x1fffc, v95
	v_add_u32_e32 v95, v18, v95
	ds_add_u32 v95, v100
	s_mov_b64 exec, s[2:3]
	s_waitcnt vmcnt(3)
	v_cndmask_b32_e64 v31, -1, v5, s[34:35]
	s_and_b64 exec, s[2:3], s[34:35]
	v_lshrrev_b32_e32 v96, 15, v31
	v_and_b32_e32 v96, 0x1fffc, v96
	v_add_u32_e32 v96, v18, v96
	ds_add_u32 v96, v100
	s_mov_b64 exec, s[2:3]
	s_waitcnt vmcnt(2)
	v_cndmask_b32_e64 v32, -1, v4, s[36:37]
	s_and_b64 exec, s[2:3], s[36:37]
	v_lshrrev_b32_e32 v97, 15, v32
	v_and_b32_e32 v97, 0x1fffc, v97
	v_add_u32_e32 v97, v18, v97
	ds_add_u32 v97, v100
	s_mov_b64 exec, s[2:3]
	s_waitcnt vmcnt(1)
	v_cndmask_b32_e64 v33, -1, v3, s[6:7]
	s_mov_b64 s[38:39], s[6:7]
	s_and_b64 exec, s[2:3], s[38:39]
	v_lshrrev_b32_e32 v98, 15, v33
	v_and_b32_e32 v98, 0x1fffc, v98
	v_add_u32_e32 v98, v18, v98
	ds_add_u32 v98, v100
	s_mov_b64 exec, s[2:3]
	s_waitcnt vmcnt(0)
	v_cndmask_b32_e32 v34, -1, v2, vcc
	s_mov_b64 s[40:41], vcc
	s_and_b64 exec, s[2:3], s[40:41]
	v_lshrrev_b32_e32 v99, 15, v34
	v_and_b32_e32 v99, 0x1fffc, v99
	v_add_u32_e32 v99, v18, v99
	ds_add_u32 v99, v100
	s_mov_b64 exec, s[2:3]
	s_cmp_eq_u32 s75, 0
	s_cbranch_scc1 .Lcnt_noslots
	s_waitcnt vmcnt(0)
	v_cmp_gt_u32_e64 s[88:89], s75, v45
	s_and_b64 exec, s[2:3], s[88:89]
	v_lshrrev_b32_e32 v117, 15, v113
	v_and_b32_e32 v117, 0x1fffc, v117
	v_add_u32_e32 v117, v18, v117
	ds_add_u32 v117, v100
	s_mov_b64 exec, s[2:3]
	v_cmp_gt_u32_e64 s[88:89], s82, v45
	s_and_b64 exec, s[2:3], s[88:89]
	v_lshrrev_b32_e32 v118, 15, v114
	v_and_b32_e32 v118, 0x1fffc, v118
	v_add_u32_e32 v118, v18, v118
	ds_add_u32 v118, v100
	s_mov_b64 exec, s[2:3]
	v_cmp_gt_u32_e64 s[88:89], s95, v45
	s_and_b64 exec, s[2:3], s[88:89]
	v_lshrrev_b32_e32 v119, 15, v115
	v_and_b32_e32 v119, 0x1fffc, v119
	v_add_u32_e32 v119, v18, v119
	ds_add_u32 v119, v100
	s_mov_b64 exec, s[2:3]
	v_cmp_gt_u32_e64 s[88:89], s32, v45
	s_and_b64 exec, s[2:3], s[88:89]
	v_lshrrev_b32_e32 v120, 15, v116
	v_and_b32_e32 v120, 0x1fffc, v120
	v_add_u32_e32 v120, v18, v120
	ds_add_u32 v120, v100
	s_mov_b64 exec, s[2:3]
.Lcnt_noslots:
	s_mov_b32 s89, s42
	s_mov_b32 s90, s43
	s_cmp_lg_u32 s94, 0
	s_cselect_b64 s[42:43], -1, 0
	s_and_b64 vcc, exec, s[42:43]
	s_cbranch_vccz .LBB2_99
	v_lshlrev_b32_e32 v2, 2, v48
	v_add_u32_e32 v7, 0x17450, v2
	v_or_b32_e32 v4, 64, v45
	v_add_u32_e32 v5, 0x17850, v2
	s_cmp_le_u32 s89, 64
	s_cbranch_scc1 .LBB2_53
	ds_read_b32 v8, v7
	s_waitcnt lgkmcnt(0)
	v_cmp_lt_u32_e32 vcc, v4, v8
	s_and_saveexec_b64 s[2:3], vcc
	s_cbranch_execz .LBB2_53
	ds_read_b32 v9, v5
	s_mov_b64 s[6:7], 0
	v_mov_b32_e32 v3, 0
	v_mov_b32_e32 v10, 1
	v_mov_b32_e32 v11, v4

.LBB2_135:
	s_or_b64 exec, exec, s[2:3]
	s_waitcnt lgkmcnt(3)
	v_add_u32_e32 v14, v15, v14
	v_add_u32_e32 v14, v14, v16
	v_add_u32_e32 v14, v14, v17
	s_waitcnt lgkmcnt(2)
	v_add_u32_e32 v6, v14, v6
	v_add_u32_e32 v6, v6, v7
	v_add_u32_e32 v6, v6, v8
	v_add_u32_e32 v6, v6, v9
	s_waitcnt lgkmcnt(1)
	v_add_u32_e32 v6, v6, v10
	v_add_u32_e32 v6, v6, v11
	v_add_u32_e32 v6, v6, v12
	v_add_u32_e32 v6, v6, v13
	s_waitcnt lgkmcnt(0)
	v_add_u32_e32 v2, v6, v2
	v_add_u32_e32 v2, v2, v3
	v_add_u32_e32 v2, v2, v4
	v_add_u32_e32 v2, v2, v5
	s_and_saveexec_b64 s[2:3], s[44:45]
	v_mov_b32_e32 v3, 0x17440
	ds_write_b32 v3, v2
	s_or_b64 exec, exec, s[2:3]
	s_movk_i32 s2, 0x4000
	v_cmp_lt_u32_e64 s[6:7], s2, v2
	s_movk_i32 s2, 0x4001
	v_cmp_gt_u32_e64 s[4:5], s2, v2
	s_mov_b64 s[2:3], -1
	s_and_b64 vcc, exec, s[4:5]
	s_waitcnt lgkmcnt(0)
	s_barrier
	s_cbranch_vccz .LBB2_252
	v_mov_b32_e32 v3, 1
	s_mov_b64 s[2:3], exec
	s_and_b64 exec, s[2:3], s[20:21]
	ds_add_rtn_u32 v66, v84, v3
	s_and_b64 exec, s[2:3], s[8:9]
	ds_add_rtn_u32 v67, v85, v3
	s_and_b64 exec, s[2:3], s[10:11]
	ds_add_rtn_u32 v68, v86, v3
	s_and_b64 exec, s[2:3], s[12:13]
	ds_add_rtn_u32 v69, v87, v3
	s_and_b64 exec, s[2:3], s[14:15]
	ds_add_rtn_u32 v70, v88, v3
	s_and_b64 exec, s[2:3], s[16:17]
	ds_add_rtn_u32 v71, v89, v3
	s_and_b64 exec, s[2:3], s[18:19]
	ds_add_rtn_u32 v72, v90, v3
	s_and_b64 exec, s[2:3], s[22:23]
	ds_add_rtn_u32 v73, v91, v3
	s_and_b64 exec, s[2:3], s[20:21]
	s_waitcnt lgkmcnt(7)
	v_lshlrev_b32_e32 v66, 2, v66
	ds_write_b32 v66, v19
	s_and_b64 exec, s[2:3], s[8:9]
	s_waitcnt lgkmcnt(7)
	v_lshlrev_b32_e32 v67, 2, v67
	ds_write_b32 v67, v20
	s_and_b64 exec, s[2:3], s[10:11]
	s_waitcnt lgkmcnt(7)
	v_lshlrev_b32_e32 v68, 2, v68
	ds_write_b32 v68, v21
	s_and_b64 exec, s[2:3], s[12:13]
	s_waitcnt lgkmcnt(7)
	v_lshlrev_b32_e32 v69, 2, v69
	ds_write_b32 v69, v22
	s_and_b64 exec, s[2:3], s[14:15]
	s_waitcnt lgkmcnt(7)
	v_lshlrev_b32_e32 v70, 2, v70
	ds_write_b32 v70, v23
	s_and_b64 exec, s[2:3], s[16:17]
	s_waitcnt lgkmcnt(7)
	v_lshlrev_b32_e32 v71, 2, v71
	ds_write_b32 v71, v24
	s_and_b64 exec, s[2:3], s[18:19]
	s_waitcnt lgkmcnt(7)
	v_lshlrev_b32_e32 v72, 2, v72
	ds_write_b32 v72, v25
	s_and_b64 exec, s[2:3], s[22:23]
	s_waitcnt lgkmcnt(7)
	v_lshlrev_b32_e32 v73, 2, v73
	ds_write_b32 v73, v26
	s_waitcnt lgkmcnt(6)
	s_and_b64 exec, s[2:3], s[24:25]
	ds_add_rtn_u32 v74, v92, v3
	s_and_b64 exec, s[2:3], s[26:27]
	ds_add_rtn_u32 v75, v93, v3
	s_and_b64 exec, s[2:3], s[28:29]
	ds_add_rtn_u32 v76, v94, v3
	s_and_b64 exec, s[2:3], s[30:31]
	ds_add_rtn_u32 v77, v95, v3
	s_and_b64 exec, s[2:3], s[34:35]
	ds_add_rtn_u32 v78, v96, v3
	s_and_b64 exec, s[2:3], s[36:37]
	ds_add_rtn_u32 v79, v97, v3
	s_and_b64 exec, s[2:3], s[38:39]
	ds_add_rtn_u32 v80, v98, v3
	s_and_b64 exec, s[2:3], s[40:41]
	ds_add_rtn_u32 v81, v99, v3
	s_and_b64 exec, s[2:3], s[24:25]
	s_waitcnt lgkmcnt(7)
	v_lshlrev_b32_e32 v74, 2, v74
	ds_write_b32 v74, v27
	s_and_b64 exec, s[2:3], s[26:27]
	s_waitcnt lgkmcnt(7)
	v_lshlrev_b32_e32 v75, 2, v75
	ds_write_b32 v75, v28
	s_and_b64 exec, s[2:3], s[28:29]
	s_waitcnt lgkmcnt(7)
	v_lshlrev_b32_e32 v76, 2, v76
	ds_write_b32 v76, v29
	s_and_b64 exec, s[2:3], s[30:31]
	s_waitcnt lgkmcnt(7)
	v_lshlrev_b32_e32 v77, 2, v77
	ds_write_b32 v77, v30
	s_and_b64 exec, s[2:3], s[34:35]
	s_waitcnt lgkmcnt(7)
	v_lshlrev_b32_e32 v78, 2, v78
	ds_write_b32 v78, v31
	s_and_b64 exec, s[2:3], s[36:37]
	s_waitcnt lgkmcnt(7)
	v_lshlrev_b32_e32 v79, 2, v79
	ds_write_b32 v79, v32
	s_and_b64 exec, s[2:3], s[38:39]
	s_waitcnt lgkmcnt(7)
	v_lshlrev_b32_e32 v80, 2, v80
	ds_write_b32 v80, v33
	s_and_b64 exec, s[2:3], s[40:41]
	s_waitcnt lgkmcnt(7)
	v_lshlrev_b32_e32 v81, 2, v81
	ds_write_b32 v81, v34
	s_cmp_eq_u32 s75, 0
	s_cbranch_scc1 .Lms_noslots
	v_cmp_gt_u32_e64 s[88:89], s75, v45
	s_and_b64 exec, s[2:3], s[88:89]
	ds_add_rtn_u32 v82, v117, v3
	s_waitcnt lgkmcnt(0)
	v_lshlrev_b32_e32 v82, 2, v82
	ds_write_b32 v82, v113
	v_cmp_gt_u32_e64 s[88:89], s82, v45
	s_and_b64 exec, s[2:3], s[88:89]
	ds_add_rtn_u32 v82, v118, v3
	s_waitcnt lgkmcnt(0)
	v_lshlrev_b32_e32 v82, 2, v82
	ds_write_b32 v82, v114
	v_cmp_gt_u32_e64 s[88:89], s95, v45
	s_and_b64 exec, s[2:3], s[88:89]
	ds_add_rtn_u32 v82, v119, v3
	s_waitcnt lgkmcnt(0)
	v_lshlrev_b32_e32 v82, 2, v82
	ds_write_b32 v82, v115
	v_cmp_gt_u32_e64 s[88:89], s32, v45
	s_and_b64 exec, s[2:3], s[88:89]
	ds_add_rtn_u32 v82, v120, v3
	s_waitcnt lgkmcnt(0)
	v_lshlrev_b32_e32 v82, 2, v82
	ds_write_b32 v82, v116
.Lms_noslots:
	s_mov_b64 exec, s[2:3]
	s_and_b64 vcc, exec, s[42:43]
	s_cbranch_vccz .LBB2_251
